# speedup vs baseline: 1.0588x; 1.0305x over previous
.LBB3_30:
	s_or_b64 exec, exec, s[12:13]
	v_xor_b32_e32 v1, 32, v24
	v_lshlrev_b32_e32 v1, 2, v1
	v_xor_b32_e32 v102, 16, v24
	v_lshlrev_b32_e32 v102, 2, v102
	v_max_f32_dpp v38, v38, v38 quad_perm:[1,0,3,2] row_mask:0xf bank_mask:0xf
	v_max_f32_dpp v37, v37, v37 quad_perm:[1,0,3,2] row_mask:0xf bank_mask:0xf
	s_nop 0
	v_max_f32_dpp v38, v38, v38 quad_perm:[2,3,0,1] row_mask:0xf bank_mask:0xf
	v_max_f32_dpp v37, v37, v37 quad_perm:[2,3,0,1] row_mask:0xf bank_mask:0xf
	s_nop 0
	v_max_f32_dpp v38, v38, v38 row_half_mirror row_mask:0xf bank_mask:0xf
	v_max_f32_dpp v37, v37, v37 row_half_mirror row_mask:0xf bank_mask:0xf
	s_nop 0
	v_max_f32_dpp v38, v38, v38 row_mirror row_mask:0xf bank_mask:0xf
	v_max_f32_dpp v37, v37, v37 row_mirror row_mask:0xf bank_mask:0xf
	s_nop 0
	v_max_f32_dpp v38, v38, v38 row_bcast:15 row_mask:0xa bank_mask:0xf
	v_max_f32_dpp v37, v37, v37 row_bcast:15 row_mask:0xa bank_mask:0xf
	s_nop 0
	v_max_f32_dpp v38, v38, v38 row_bcast:31 row_mask:0xc bank_mask:0xf
	v_max_f32_dpp v37, v37, v37 row_bcast:31 row_mask:0xc bank_mask:0xf
	s_nop 0
	v_readlane_b32 s14, v38, 63
	v_readlane_b32 s15, v37, 63
	v_lshlrev_b32_e32 v39, 2, v19
	v_or_b32_e32 v40, 0x22bc0, v39
	v_or_b32_e32 v39, 0x22c00, v39
	v_mov_b32_e32 v41, s15
	v_mov_b32_e32 v42, s14
	s_and_saveexec_b64 s[12:13], s[4:5]
	ds_write_b32 v40, v41
	ds_write_b32 v39, v42
.LBB3_32:
	s_or_b64 exec, exec, s[12:13]
	v_mov_b32_e32 v37, 0x22bc0
	s_waitcnt lgkmcnt(0)
	s_barrier
	ds_read_b128 v[38:41], v37
	v_mov_b32_e32 v37, 0x22c00
	ds_read_b128 v[42:45], v37
	s_movk_i32 s12, 0xfc
	s_waitcnt lgkmcnt(1)
	v_max_f32_e32 v37, v39, v39
	v_max_f32_e32 v38, v38, v38
	s_waitcnt lgkmcnt(0)
	v_max_f32_e32 v39, v42, v42
	v_mov_b32_e32 v42, 0x22bd0
	v_max_f32_e32 v37, v38, v37
	v_max_f32_e32 v38, v43, v43
	v_mov_b32_e32 v43, 0x22c10
	ds_read_b128 v[46:49], v42
	ds_read_b128 v[50:53], v43
	v_max_f32_e32 v38, v39, v38
	v_max3_f32 v38, v38, v44, v45
	v_max3_f32 v37, v37, v40, v41
	s_waitcnt lgkmcnt(1)
	v_max3_f32 v37, v37, v46, v47
	s_waitcnt lgkmcnt(0)
	v_max3_f32 v42, v38, v50, v51
	v_mov_b32_e32 v38, 0x22be0
	ds_read_b128 v[38:41], v38
	v_max3_f32 v54, v42, v52, v53
	v_mov_b32_e32 v42, 0x22c20
	v_max3_f32 v37, v37, v48, v49
	ds_read_b128 v[42:45], v42
	s_waitcnt lgkmcnt(1)
	v_max3_f32 v37, v37, v38, v39
	v_mov_b32_e32 v38, 0x22bf0
	v_mov_b32_e32 v39, 0x22c30
	ds_read_b128 v[46:49], v38
	ds_read_b128 v[50:53], v39
	s_waitcnt lgkmcnt(2)
	v_max3_f32 v38, v54, v42, v43
	v_max3_f32 v37, v37, v40, v41
	v_max3_f32 v38, v38, v44, v45
	s_waitcnt lgkmcnt(1)
	v_max3_f32 v37, v37, v46, v47
	s_waitcnt lgkmcnt(0)
	v_max3_f32 v39, v38, v50, v51
	v_max3_f32 v38, v37, v48, v49
	v_max3_f32 v39, v39, v52, v53
	v_and_b32_e32 v41, 0x7fffffff, v12
	v_and_b32_e32 v40, 0x7fffffff, v14
	v_pk_mul_f32 v[40:41], v[38:39], v[40:41]
	s_nop 0
	v_add_f32_e32 v37, v40, v41
	v_and_b32_e32 v41, 0x7fffffff, v13
	v_and_b32_e32 v40, 0x7fffffff, v15
	v_pk_mul_f32 v[40:41], v[38:39], v[40:41]
	v_add_f32_e64 v37, |v16|, v37
	v_add_f32_e32 v40, v40, v41
	v_add_f32_e64 v40, |v17|, v40
	v_max3_f32 v37, v37, 0, v40
	v_and_b32_e32 v41, 0x7fffffff, v6
	v_and_b32_e32 v40, 0x7fffffff, v8
	v_pk_mul_f32 v[40:41], v[38:39], v[40:41]
	s_nop 0
	v_add_f32_e32 v40, v40, v41
	v_add_f32_e64 v42, |v10|, v40
	v_and_b32_e32 v41, 0x7fffffff, v7
	v_and_b32_e32 v40, 0x7fffffff, v9
	v_pk_mul_f32 v[38:39], v[38:39], v[40:41]
	s_nop 0
	v_add_f32_e32 v38, v38, v39
	v_add_f32_e64 v38, |v11|, v38
	v_max3_f32 v37, v37, v42, v38
	v_max_f32_dpp v37, v37, v37 quad_perm:[1,0,3,2] row_mask:0xf bank_mask:0xf
	s_nop 1
	v_max_f32_dpp v37, v37, v37 quad_perm:[2,3,0,1] row_mask:0xf bank_mask:0xf
	s_nop 1
	v_max_f32_dpp v37, v37, v37 row_half_mirror row_mask:0xf bank_mask:0xf
	s_nop 1
	v_max_f32_dpp v37, v37, v37 row_mirror row_mask:0xf bank_mask:0xf
	s_nop 1
	v_max_f32_dpp v37, v37, v37 row_bcast:15 row_mask:0xa bank_mask:0xf
	s_nop 1
	v_max_f32_dpp v37, v37, v37 row_bcast:31 row_mask:0xc bank_mask:0xf
	s_nop 1
	v_readlane_b32 s14, v37, 63
	v_mov_b32_e32 v36, 0x800000
	s_nop 1
	v_mov_b32_e32 v2, s14
	v_bfe_u32 v3, v2, 23, 8
	v_lshlrev_b32_e32 v24, 23, v3
	v_sub_u32_e32 v24, 0x7e000000, v24
	v_cmp_gt_u32_e32 vcc, s12, v3
	v_cmp_neq_f32_e64 s[12:13], 0, v2
	s_nop 0
	v_cndmask_b32_e32 v3, v36, v24, vcc
	s_andn2_b64 vcc, exec, s[28:29]
	v_cndmask_b32_e64 v2, 1.0, v3, s[12:13]
	s_cbranch_vccnz .LBB3_39
	s_and_saveexec_b64 s[12:13], s[10:11]
	s_cbranch_execnz .LBB3_114
	s_or_b64 exec, exec, s[12:13]
	s_and_saveexec_b64 s[10:11], s[8:9]
	s_cbranch_execnz .LBB3_115

.Lskip_stage:
	s_or_b64 exec, exec, s[34:35]
	s_waitcnt lgkmcnt(0)
	s_barrier
	s_and_b64 vcc, exec, s[6:7]
	s_cbranch_vccz .LBB3_43
	v_sub_u32_e32 v61, 0x7f000000, v20
	v_and_b32_e32 v63, 31, v18
	v_lshlrev_b32_e32 v10, 2, v63
	v_add_u32_e32 v10, 0x24870, v10
	ds_read_b32 v64, v10 offset:0
	ds_read_b32 v66, v10 offset:1024
	ds_read_b32 v68, v10 offset:128
	ds_read_b32 v70, v10 offset:1152
	ds_read_b32 v72, v10 offset:256
	ds_read_b32 v74, v10 offset:1280
	ds_read_b32 v76, v10 offset:384
	ds_read_b32 v78, v10 offset:1408
	ds_read_b32 v80, v10 offset:512
	ds_read_b32 v82, v10 offset:1536
	ds_read_b32 v84, v10 offset:640
	ds_read_b32 v86, v10 offset:1664
	ds_read_b32 v88, v10 offset:768
	ds_read_b32 v90, v10 offset:1792
	ds_read_b32 v92, v10 offset:896
	ds_read_b32 v94, v10 offset:1920
	s_waitcnt lgkmcnt(0)
	v_mul_f32_e32 v66, v61, v66
	v_cvt_pk_f16_f32 v65, v66, 0
	v_mov_b32_e32 v66, 0
	v_mov_b32_e32 v67, 0
	v_mul_f32_e32 v70, v61, v70
	v_cvt_pk_f16_f32 v69, v70, 0
	v_mov_b32_e32 v70, 0
	v_mov_b32_e32 v71, 0
	v_mul_f32_e32 v74, v61, v74
	v_cvt_pk_f16_f32 v73, v74, 0
	v_mov_b32_e32 v74, 0
	v_mov_b32_e32 v75, 0
	v_mul_f32_e32 v78, v61, v78
	v_cvt_pk_f16_f32 v77, v78, 0
	v_mov_b32_e32 v78, 0
	v_mov_b32_e32 v79, 0
	v_mul_f32_e32 v82, v61, v82
	v_cvt_pk_f16_f32 v81, v82, 0
	v_mov_b32_e32 v82, 0
	v_mov_b32_e32 v83, 0
	v_mul_f32_e32 v86, v61, v86
	v_cvt_pk_f16_f32 v85, v86, 0
	v_mov_b32_e32 v86, 0
	v_mov_b32_e32 v87, 0
	v_mul_f32_e32 v90, v61, v90
	v_cvt_pk_f16_f32 v89, v90, 0
	v_mov_b32_e32 v90, 0
	v_mov_b32_e32 v91, 0
	v_mul_f32_e32 v94, v61, v94
	v_cvt_pk_f16_f32 v93, v94, 0
	v_mov_b32_e32 v94, 0
	v_mov_b32_e32 v95, 0
	v_and_b32_e32 v63, 31, v18
	v_lshrrev_b32_e32 v55, 3, v63
	v_lshlrev_b32_e32 v56, 2, v55
	v_and_b32_e32 v57, 3, v63
	v_add_u32_e32 v56, v56, v57
	v_lshlrev_b32_e32 v55, 4, v55
	v_bfe_u32 v57, v63, 1, 1
	v_lshl_add_u32 v55, v57, 3, v55
	v_and_b32_e32 v57, 1, v63
	v_cmp_eq_u32_e32 vcc, 1, v57
	v_mov_b32_e32 v57, 0x5040100
	v_mov_b32_e32 v10, 0x7060302
	v_lshlrev_b32_e32 v58, 1, v63
	v_cndmask_b32_e32 v57, v57, v10, vcc
	v_mov_b32_e32 v59, 0x22c50
	v_mov_b32_e32 v60, 1
	v_mov_b32_e32 v62, 0x3c003c00
	v_mov_b32_e32 v34, 0
	v_mov_b32_e32 v35, 0
	s_mov_b32 s54, 0xf0f0f0f0
	s_mov_b32 s55, 0
	s_mov_b32 s56, 0
	s_mov_b32 s57, -1
	s_mov_b32 s64, 0x24160
	s_mov_b32 s65, 0x244e0
	s_movk_i32 s49, 0x210
	v_mov_b32_e32 v50, 0x24860
	v_mov_b32_e32 v51, 0x244e0
	v_mov_b32_e32 v52, 0x24160
	v_lshrrev_b32_e32 v10, 2, v0
	v_and_b32_e32 v17, 3, v0
	v_mov_b32_e32 v40, 0
	v_mov_b32_e32 v41, 0
	v_mov_b32_e32 v42, 0
	v_mov_b32_e32 v43, 0
	v_cmp_gt_u32_e32 vcc, s3, v10
	s_and_saveexec_b64 s[58:59], vcc
	s_cbranch_execz .Llin_skip
	v_lshlrev_b32_e32 v11, 2, v10
	v_add_u32_e32 v12, 0x228a0, v11
	v_add_u32_e32 v13, 0x22580, v11
	ds_read2_b32 v[14:15], v12 offset1:1
	ds_read_b32 v43, v13
	s_waitcnt lgkmcnt(0)
	v_sub_u32_e32 v42, v15, v14
	v_add_u32_e32 v14, 3, v42
	v_lshrrev_b32_e32 v14, 2, v14
	v_add_u32_e32 v15, v43, v14
	v_add_u32_e32 v16, v43, v17
	v_mov_b32_e32 v13, 0x1ce00

.Llin_skip:
	s_mov_b64 exec, s[58:59]
	s_nop 4
	v_add_f32_dpp v40, v40, v40 quad_perm:[1,0,3,2] row_mask:0xf bank_mask:0xf
	v_add_f32_dpp v41, v41, v41 quad_perm:[1,0,3,2] row_mask:0xf bank_mask:0xf
	s_nop 1
	v_add_f32_dpp v40, v40, v40 quad_perm:[2,3,0,1] row_mask:0xf bank_mask:0xf
	v_add_f32_dpp v41, v41, v41 quad_perm:[2,3,0,1] row_mask:0xf bank_mask:0xf
	v_cmp_eq_u32_e32 vcc, 0, v17
	s_movk_i32 s45, 0xe0
	v_cmp_gt_u32_e64 s[60:61], s45, v10
	v_add_u32_e32 v11, -1, v42
	v_ffbh_u32_e32 v11, v11
	s_and_b64 vcc, vcc, s[60:61]
	s_and_saveexec_b64 s[60:61], vcc
	v_sub_u32_e32 v11, 32, v11
	v_cmp_lt_u32_e32 vcc, 1, v42
	v_lshlrev_b32_e32 v44, 4, v43
	v_add_u32_e32 v44, 0x1ce00, v44
	v_cndmask_b32_e32 v11, 0, v11, vcc
	v_lshlrev_b32_e32 v11, 23, v11
	v_mov_b32_e32 v45, v42
	v_sub_u32_e32 v49, 0x46800000, v11
	v_add_u32_e32 v12, 0x38000000, v11
	v_cvt_f32_u32_e32 v48, v42
	v_mul_f32_e32 v12, v12, v20
	v_mul_f32_e32 v46, v40, v49
	v_mul_f32_e32 v47, v41, v49
	v_mul_f32_e32 v48, v48, v49
	v_lshlrev_b32_e32 v13, 3, v10
	v_add_u32_e32 v13, 0x22c60, v13
	ds_write_b64 v13, v[44:45]
	v_lshlrev_b32_e32 v13, 4, v10
	v_add_u32_e32 v13, 0x23360, v13
	ds_write_b128 v13, v[46:49]
	v_lshlrev_b32_e32 v13, 2, v10
	v_add_u32_e32 v13, 0x22200, v13
	ds_write_b32 v13, v12
	v_cmp_gt_u32_e32 vcc, s3, v10
	v_cmp_lt_u32_e64 s[46:47], 16, v42
	s_and_b64 s[38:39], exec, vcc
	s_and_b64 s[40:41], s[38:39], s[46:47]
	s_andn2_b64 s[38:39], s[38:39], s[46:47]
	s_bcnt1_i32_b64 s42, s[40:41]
	s_bcnt1_i32_b64 s43, s[38:39]
	s_mov_b64 exec, 1
	v_mov_b32_e32 v14, s42
	v_mov_b32_e32 v15, s43
	ds_add_rtn_u32 v16, v50, v14
	ds_add_rtn_u32 v38, v50, v15 offset:4
	s_waitcnt lgkmcnt(0)
	v_readfirstlane_b32 s42, v16
	v_readfirstlane_b32 s43, v38
	s_mov_b64 exec, s[40:41]
	v_mbcnt_lo_u32_b32 v14, s40, 0
	v_mbcnt_hi_u32_b32 v14, s41, v14
	v_add_u32_e32 v14, s42, v14
	v_lshl_add_u32 v14, v14, 2, v52
	ds_write_b32 v14, v10
	s_mov_b64 exec, s[38:39]
	v_mbcnt_lo_u32_b32 v14, s38, 0
	v_mbcnt_hi_u32_b32 v14, s39, v14
	v_add_u32_e32 v14, s43, v14
	v_lshl_add_u32 v14, v14, 2, v51
	ds_write_b32 v14, v10
	s_mov_b64 exec, s[60:61]
	s_waitcnt lgkmcnt(0)
	s_barrier
	v_mov_b32_e32 v11, 0x24860
	ds_read_b64 v[12:13], v11
	v_mov_b32_e32 v61, 0x22c60
	v_mov_b32_e32 v62, 0x23360
	v_cmp_gt_u32_e32 vcc, 32, v18
	v_mov_b32_e32 v2, v55
	s_nop 0
	v_cndmask_b32_e64 v63, 0, -1, vcc
	s_waitcnt lgkmcnt(0)
	v_readfirstlane_b32 s62, v12
	v_readfirstlane_b32 s63, v13
	s_add_i32 s62, s62, 1
	s_lshr_b32 s62, s62, 1
	s_add_i32 s63, s63, 1
	s_lshr_b32 s63, s63, 1
.Lp_next:
	s_mov_b64 exec, 1
	ds_add_rtn_u32 v10, v59, v60
	s_mov_b64 exec, -1
	s_waitcnt lgkmcnt(0)
	v_readfirstlane_b32 s34, v10
	s_cmp_lt_u32 s34, s62
	s_cselect_b32 s45, s64, s65
	s_cselect_b32 s46, 0, s62
	s_cselect_b32 s48, s62, s63
	s_sub_u32 s47, s34, s46
	s_cmp_ge_u32 s47, s48
	s_cbranch_scc1 .Lp_done
	s_lshl_b32 s47, s47, 3
	s_add_u32 s45, s45, s47
	v_mov_b32_e32 v11, s45
	ds_read2_b32 v[12:13], v11 offset1:1
	s_waitcnt lgkmcnt(0)
	v_readfirstlane_b32 s35, v12
	v_readfirstlane_b32 s36, v13
	s_nop 1
	v_mov_b32_e32 v10, s35
	v_mov_b32_e32 v11, s36
	v_cndmask_b32_e64 v12, v10, v11, s[54:55]
	v_cndmask_b32_e64 v13, v10, v11, s[56:57]
	v_lshl_add_u32 v12, v12, 3, v61
	v_lshl_add_u32 v14, v13, 4, v62
	ds_read_b64 v[2:3], v12
	ds_read_b128 v[4:7], v14
	v_mad_u32_u24 v9, v13, s49, v58
	v_mov_b32_e32 v8, v56
	s_waitcnt lgkmcnt(0)
	v_add_u32_e32 v2, v2, v55
	v_and_b32_e32 v3, v3, v63
	s_nop 0
	v_readlane_b32 s41, v3, 0
	v_readlane_b32 s42, v3, 4
	s_max_u32 s43, s41, s42
	s_cmp_eq_u32 s43, 0
	s_cbranch_scc1 .Lp_zero
	ds_read_b64 v[36:37], v2
	v_cmp_gt_u32_e32 vcc, v3, v8
	v_add_u32_e32 v2, 64, v2
	v_add_u32_e32 v8, 16, v8
	v_mov_b32_e32 v33, 0x3c00
	s_waitcnt lgkmcnt(0)
	v_perm_b32 v32, v37, v36, v57
	v_cndmask_b32_e32 v33, 0, v33, vcc
	s_nop 0
	v_cndmask_b32_e32 v32, 0, v32, vcc
	s_nop 1
	v_mfma_f32_32x32x16_f16 v[96:111], v[32:35], v[64:67], 0
	v_mfma_f32_32x32x16_f16 v[112:127], v[32:35], v[68:71], 0
	s_nop 10
	s_mov_b32 s45, s43
	s_min_u32 s46, s45, 16
	s_add_i32 s46, s46, 3
	s_lshr_b32 s46, s46, 2
	s_cmp_eq_u32 s46, 4
	s_cbranch_scc1 .Lf4
	s_cmp_eq_u32 s46, 3
	s_cbranch_scc1 .Lf3
	s_cmp_eq_u32 s46, 2
	s_cbranch_scc1 .Lf2
.Lf1:
	v_add_f32_e64 v38, |v96|, |v97|
	v_add_f32_e64 v39, |v98|, |v99|
	v_add_f32_e32 v24, v38, v39
	s_nop 8
	v_mfma_f32_32x32x16_f16 v[96:111], v[32:35], v[72:75], 0
	v_add_f32_e64 v38, |v112|, |v113|
	v_add_f32_e64 v39, |v114|, |v115|
	v_add_f32_e32 v25, v38, v39
	s_nop 8
	v_mfma_f32_32x32x16_f16 v[112:127], v[32:35], v[76:79], 0
	v_add_f32_e64 v38, |v96|, |v97|
	v_add_f32_e64 v39, |v98|, |v99|
	v_add_f32_e32 v26, v38, v39
	s_nop 8
	v_mfma_f32_32x32x16_f16 v[96:111], v[32:35], v[80:83], 0
	v_add_f32_e64 v38, |v112|, |v113|
	v_add_f32_e64 v39, |v114|, |v115|
	v_add_f32_e32 v27, v38, v39
	s_nop 8
	v_mfma_f32_32x32x16_f16 v[112:127], v[32:35], v[84:87], 0
	v_add_f32_e64 v38, |v96|, |v97|
	v_add_f32_e64 v39, |v98|, |v99|
	v_add_f32_e32 v28, v38, v39
	s_nop 8
	v_mfma_f32_32x32x16_f16 v[96:111], v[32:35], v[88:91], 0
	v_add_f32_e64 v38, |v112|, |v113|
	v_add_f32_e64 v39, |v114|, |v115|
	v_add_f32_e32 v29, v38, v39
	s_nop 8
	v_mfma_f32_32x32x16_f16 v[112:127], v[32:35], v[92:95], 0
	v_add_f32_e64 v38, |v96|, |v97|
	v_add_f32_e64 v39, |v98|, |v99|
	v_add_f32_e32 v30, v38, v39
	s_nop 8
	v_add_f32_e64 v38, |v112|, |v113|
	v_add_f32_e64 v39, |v114|, |v115|
	v_add_f32_e32 v31, v38, v39
	s_nop 8
	s_branch .Lafter_first
.Lf2:
	v_add_f32_e64 v38, |v96|, |v97|
	v_add_f32_e64 v39, |v98|, |v99|
	v_add_f32_e64 v38, v38, |v100|
	v_add_f32_e64 v39, v39, |v101|
	v_add_f32_e64 v38, v38, |v102|
	v_add_f32_e64 v39, v39, |v103|
	v_add_f32_e32 v24, v38, v39
	s_nop 4
	v_mfma_f32_32x32x16_f16 v[96:111], v[32:35], v[72:75], 0
	v_add_f32_e64 v38, |v112|, |v113|
	v_add_f32_e64 v39, |v114|, |v115|
	v_add_f32_e64 v38, v38, |v116|
	v_add_f32_e64 v39, v39, |v117|
	v_add_f32_e64 v38, v38, |v118|
	v_add_f32_e64 v39, v39, |v119|
	v_add_f32_e32 v25, v38, v39
	s_nop 4
	v_mfma_f32_32x32x16_f16 v[112:127], v[32:35], v[76:79], 0
	v_add_f32_e64 v38, |v96|, |v97|
	v_add_f32_e64 v39, |v98|, |v99|
	v_add_f32_e64 v38, v38, |v100|
	v_add_f32_e64 v39, v39, |v101|
	v_add_f32_e64 v38, v38, |v102|
	v_add_f32_e64 v39, v39, |v103|
	v_add_f32_e32 v26, v38, v39
	s_nop 4
	v_mfma_f32_32x32x16_f16 v[96:111], v[32:35], v[80:83], 0
	v_add_f32_e64 v38, |v112|, |v113|
	v_add_f32_e64 v39, |v114|, |v115|
	v_add_f32_e64 v38, v38, |v116|
	v_add_f32_e64 v39, v39, |v117|
	v_add_f32_e64 v38, v38, |v118|
	v_add_f32_e64 v39, v39, |v119|
	v_add_f32_e32 v27, v38, v39
	s_nop 4
	v_mfma_f32_32x32x16_f16 v[112:127], v[32:35], v[84:87], 0
	v_add_f32_e64 v38, |v96|, |v97|
	v_add_f32_e64 v39, |v98|, |v99|
	v_add_f32_e64 v38, v38, |v100|
	v_add_f32_e64 v39, v39, |v101|
	v_add_f32_e64 v38, v38, |v102|
	v_add_f32_e64 v39, v39, |v103|
	v_add_f32_e32 v28, v38, v39
	s_nop 4
	v_mfma_f32_32x32x16_f16 v[96:111], v[32:35], v[88:91], 0
	v_add_f32_e64 v38, |v112|, |v113|
	v_add_f32_e64 v39, |v114|, |v115|
	v_add_f32_e64 v38, v38, |v116|
	v_add_f32_e64 v39, v39, |v117|
	v_add_f32_e64 v38, v38, |v118|
	v_add_f32_e64 v39, v39, |v119|
	v_add_f32_e32 v29, v38, v39
	s_nop 4
	v_mfma_f32_32x32x16_f16 v[112:127], v[32:35], v[92:95], 0
	v_add_f32_e64 v38, |v96|, |v97|
	v_add_f32_e64 v39, |v98|, |v99|
	v_add_f32_e64 v38, v38, |v100|
	v_add_f32_e64 v39, v39, |v101|
	v_add_f32_e64 v38, v38, |v102|
	v_add_f32_e64 v39, v39, |v103|
	v_add_f32_e32 v30, v38, v39
	s_nop 4
	v_add_f32_e64 v38, |v112|, |v113|
	v_add_f32_e64 v39, |v114|, |v115|
	v_add_f32_e64 v38, v38, |v116|
	v_add_f32_e64 v39, v39, |v117|
	v_add_f32_e64 v38, v38, |v118|
	v_add_f32_e64 v39, v39, |v119|
	v_add_f32_e32 v31, v38, v39
	s_nop 4
	s_branch .Lafter_first
.Lf3:
	v_add_f32_e64 v38, |v96|, |v97|
	v_add_f32_e64 v39, |v98|, |v99|
	v_add_f32_e64 v38, v38, |v100|
	v_add_f32_e64 v39, v39, |v101|
	v_add_f32_e64 v38, v38, |v102|
	v_add_f32_e64 v39, v39, |v103|
	v_add_f32_e64 v38, v38, |v104|
	v_add_f32_e64 v39, v39, |v105|
	v_add_f32_e64 v38, v38, |v106|
	v_add_f32_e64 v39, v39, |v107|
	v_add_f32_e32 v24, v38, v39
	s_nop 0
	v_mfma_f32_32x32x16_f16 v[96:111], v[32:35], v[72:75], 0
	v_add_f32_e64 v38, |v112|, |v113|
	v_add_f32_e64 v39, |v114|, |v115|
	v_add_f32_e64 v38, v38, |v116|
	v_add_f32_e64 v39, v39, |v117|
	v_add_f32_e64 v38, v38, |v118|
	v_add_f32_e64 v39, v39, |v119|
	v_add_f32_e64 v38, v38, |v120|
	v_add_f32_e64 v39, v39, |v121|
	v_add_f32_e64 v38, v38, |v122|
	v_add_f32_e64 v39, v39, |v123|
	v_add_f32_e32 v25, v38, v39
	s_nop 0
	v_mfma_f32_32x32x16_f16 v[112:127], v[32:35], v[76:79], 0
	v_add_f32_e64 v38, |v96|, |v97|
	v_add_f32_e64 v39, |v98|, |v99|
	v_add_f32_e64 v38, v38, |v100|
	v_add_f32_e64 v39, v39, |v101|
	v_add_f32_e64 v38, v38, |v102|
	v_add_f32_e64 v39, v39, |v103|
	v_add_f32_e64 v38, v38, |v104|
	v_add_f32_e64 v39, v39, |v105|
	v_add_f32_e64 v38, v38, |v106|
	v_add_f32_e64 v39, v39, |v107|
	v_add_f32_e32 v26, v38, v39
	s_nop 0
	v_mfma_f32_32x32x16_f16 v[96:111], v[32:35], v[80:83], 0
	v_add_f32_e64 v38, |v112|, |v113|
	v_add_f32_e64 v39, |v114|, |v115|
	v_add_f32_e64 v38, v38, |v116|
	v_add_f32_e64 v39, v39, |v117|
	v_add_f32_e64 v38, v38, |v118|
	v_add_f32_e64 v39, v39, |v119|
	v_add_f32_e64 v38, v38, |v120|
	v_add_f32_e64 v39, v39, |v121|
	v_add_f32_e64 v38, v38, |v122|
	v_add_f32_e64 v39, v39, |v123|
	v_add_f32_e32 v27, v38, v39
	s_nop 0
	v_mfma_f32_32x32x16_f16 v[112:127], v[32:35], v[84:87], 0
	v_add_f32_e64 v38, |v96|, |v97|
	v_add_f32_e64 v39, |v98|, |v99|
	v_add_f32_e64 v38, v38, |v100|
	v_add_f32_e64 v39, v39, |v101|
	v_add_f32_e64 v38, v38, |v102|
	v_add_f32_e64 v39, v39, |v103|
	v_add_f32_e64 v38, v38, |v104|
	v_add_f32_e64 v39, v39, |v105|
	v_add_f32_e64 v38, v38, |v106|
	v_add_f32_e64 v39, v39, |v107|
	v_add_f32_e32 v28, v38, v39
	s_nop 0
	v_mfma_f32_32x32x16_f16 v[96:111], v[32:35], v[88:91], 0
	v_add_f32_e64 v38, |v112|, |v113|
	v_add_f32_e64 v39, |v114|, |v115|
	v_add_f32_e64 v38, v38, |v116|
	v_add_f32_e64 v39, v39, |v117|
	v_add_f32_e64 v38, v38, |v118|
	v_add_f32_e64 v39, v39, |v119|
	v_add_f32_e64 v38, v38, |v120|
	v_add_f32_e64 v39, v39, |v121|
	v_add_f32_e64 v38, v38, |v122|
	v_add_f32_e64 v39, v39, |v123|
	v_add_f32_e32 v29, v38, v39
	s_nop 0
	v_mfma_f32_32x32x16_f16 v[112:127], v[32:35], v[92:95], 0
	v_add_f32_e64 v38, |v96|, |v97|
	v_add_f32_e64 v39, |v98|, |v99|
	v_add_f32_e64 v38, v38, |v100|
	v_add_f32_e64 v39, v39, |v101|
	v_add_f32_e64 v38, v38, |v102|
	v_add_f32_e64 v39, v39, |v103|
	v_add_f32_e64 v38, v38, |v104|
	v_add_f32_e64 v39, v39, |v105|
	v_add_f32_e64 v38, v38, |v106|
	v_add_f32_e64 v39, v39, |v107|
	v_add_f32_e32 v30, v38, v39
	s_nop 0
	v_add_f32_e64 v38, |v112|, |v113|
	v_add_f32_e64 v39, |v114|, |v115|
	v_add_f32_e64 v38, v38, |v116|
	v_add_f32_e64 v39, v39, |v117|
	v_add_f32_e64 v38, v38, |v118|
	v_add_f32_e64 v39, v39, |v119|
	v_add_f32_e64 v38, v38, |v120|
	v_add_f32_e64 v39, v39, |v121|
	v_add_f32_e64 v38, v38, |v122|
	v_add_f32_e64 v39, v39, |v123|
	v_add_f32_e32 v31, v38, v39
	s_nop 0
	s_branch .Lafter_first
.Lf4:
	v_add_f32_e64 v38, |v96|, |v97|
	v_add_f32_e64 v39, |v98|, |v99|
	v_add_f32_e64 v38, v38, |v100|
	v_add_f32_e64 v39, v39, |v101|
	v_add_f32_e64 v38, v38, |v102|
	v_add_f32_e64 v39, v39, |v103|
	v_add_f32_e64 v38, v38, |v104|
	v_add_f32_e64 v39, v39, |v105|
	v_add_f32_e64 v38, v38, |v106|
	v_add_f32_e64 v39, v39, |v107|
	v_add_f32_e64 v38, v38, |v108|
	v_add_f32_e64 v39, v39, |v109|
	v_add_f32_e64 v38, v38, |v110|
	v_add_f32_e64 v39, v39, |v111|
	v_add_f32_e32 v24, v38, v39
	v_mfma_f32_32x32x16_f16 v[96:111], v[32:35], v[72:75], 0
	v_add_f32_e64 v38, |v112|, |v113|
	v_add_f32_e64 v39, |v114|, |v115|
	v_add_f32_e64 v38, v38, |v116|
	v_add_f32_e64 v39, v39, |v117|
	v_add_f32_e64 v38, v38, |v118|
	v_add_f32_e64 v39, v39, |v119|
	v_add_f32_e64 v38, v38, |v120|
	v_add_f32_e64 v39, v39, |v121|
	v_add_f32_e64 v38, v38, |v122|
	v_add_f32_e64 v39, v39, |v123|
	v_add_f32_e64 v38, v38, |v124|
	v_add_f32_e64 v39, v39, |v125|
	v_add_f32_e64 v38, v38, |v126|
	v_add_f32_e64 v39, v39, |v127|
	v_add_f32_e32 v25, v38, v39
	v_mfma_f32_32x32x16_f16 v[112:127], v[32:35], v[76:79], 0
	v_add_f32_e64 v38, |v96|, |v97|
	v_add_f32_e64 v39, |v98|, |v99|
	v_add_f32_e64 v38, v38, |v100|
	v_add_f32_e64 v39, v39, |v101|
	v_add_f32_e64 v38, v38, |v102|
	v_add_f32_e64 v39, v39, |v103|
	v_add_f32_e64 v38, v38, |v104|
	v_add_f32_e64 v39, v39, |v105|
	v_add_f32_e64 v38, v38, |v106|
	v_add_f32_e64 v39, v39, |v107|
	v_add_f32_e64 v38, v38, |v108|
	v_add_f32_e64 v39, v39, |v109|
	v_add_f32_e64 v38, v38, |v110|
	v_add_f32_e64 v39, v39, |v111|
	v_add_f32_e32 v26, v38, v39
	v_mfma_f32_32x32x16_f16 v[96:111], v[32:35], v[80:83], 0
	v_add_f32_e64 v38, |v112|, |v113|
	v_add_f32_e64 v39, |v114|, |v115|
	v_add_f32_e64 v38, v38, |v116|
	v_add_f32_e64 v39, v39, |v117|
	v_add_f32_e64 v38, v38, |v118|
	v_add_f32_e64 v39, v39, |v119|
	v_add_f32_e64 v38, v38, |v120|
	v_add_f32_e64 v39, v39, |v121|
	v_add_f32_e64 v38, v38, |v122|
	v_add_f32_e64 v39, v39, |v123|
	v_add_f32_e64 v38, v38, |v124|
	v_add_f32_e64 v39, v39, |v125|
	v_add_f32_e64 v38, v38, |v126|
	v_add_f32_e64 v39, v39, |v127|
	v_add_f32_e32 v27, v38, v39
	v_mfma_f32_32x32x16_f16 v[112:127], v[32:35], v[84:87], 0
	v_add_f32_e64 v38, |v96|, |v97|
	v_add_f32_e64 v39, |v98|, |v99|
	v_add_f32_e64 v38, v38, |v100|
	v_add_f32_e64 v39, v39, |v101|
	v_add_f32_e64 v38, v38, |v102|
	v_add_f32_e64 v39, v39, |v103|
	v_add_f32_e64 v38, v38, |v104|
	v_add_f32_e64 v39, v39, |v105|
	v_add_f32_e64 v38, v38, |v106|
	v_add_f32_e64 v39, v39, |v107|
	v_add_f32_e64 v38, v38, |v108|
	v_add_f32_e64 v39, v39, |v109|
	v_add_f32_e64 v38, v38, |v110|
	v_add_f32_e64 v39, v39, |v111|
	v_add_f32_e32 v28, v38, v39
	v_mfma_f32_32x32x16_f16 v[96:111], v[32:35], v[88:91], 0
	v_add_f32_e64 v38, |v112|, |v113|
	v_add_f32_e64 v39, |v114|, |v115|
	v_add_f32_e64 v38, v38, |v116|
	v_add_f32_e64 v39, v39, |v117|
	v_add_f32_e64 v38, v38, |v118|
	v_add_f32_e64 v39, v39, |v119|
	v_add_f32_e64 v38, v38, |v120|
	v_add_f32_e64 v39, v39, |v121|
	v_add_f32_e64 v38, v38, |v122|
	v_add_f32_e64 v39, v39, |v123|
	v_add_f32_e64 v38, v38, |v124|
	v_add_f32_e64 v39, v39, |v125|
	v_add_f32_e64 v38, v38, |v126|
	v_add_f32_e64 v39, v39, |v127|
	v_add_f32_e32 v29, v38, v39
	v_mfma_f32_32x32x16_f16 v[112:127], v[32:35], v[92:95], 0
	v_add_f32_e64 v38, |v96|, |v97|
	v_add_f32_e64 v39, |v98|, |v99|
	v_add_f32_e64 v38, v38, |v100|
	v_add_f32_e64 v39, v39, |v101|
	v_add_f32_e64 v38, v38, |v102|
	v_add_f32_e64 v39, v39, |v103|
	v_add_f32_e64 v38, v38, |v104|
	v_add_f32_e64 v39, v39, |v105|
	v_add_f32_e64 v38, v38, |v106|
	v_add_f32_e64 v39, v39, |v107|
	v_add_f32_e64 v38, v38, |v108|
	v_add_f32_e64 v39, v39, |v109|
	v_add_f32_e64 v38, v38, |v110|
	v_add_f32_e64 v39, v39, |v111|
	v_add_f32_e32 v30, v38, v39
	v_add_f32_e64 v38, |v112|, |v113|
	v_add_f32_e64 v39, |v114|, |v115|
	v_add_f32_e64 v38, v38, |v116|
	v_add_f32_e64 v39, v39, |v117|
	v_add_f32_e64 v38, v38, |v118|
	v_add_f32_e64 v39, v39, |v119|
	v_add_f32_e64 v38, v38, |v120|
	v_add_f32_e64 v39, v39, |v121|
	v_add_f32_e64 v38, v38, |v122|
	v_add_f32_e64 v39, v39, |v123|
	v_add_f32_e64 v38, v38, |v124|
	v_add_f32_e64 v39, v39, |v125|
	v_add_f32_e64 v38, v38, |v126|
	v_add_f32_e64 v39, v39, |v127|
	v_add_f32_e32 v31, v38, v39
.Lafter_first:
	s_cmp_le_u32 s43, 16
	s_cbranch_scc1 .Lp_fin
	s_mov_b32 s44, 16
.Lsub:
	ds_read_b64 v[36:37], v2
	v_cmp_gt_u32_e32 vcc, v3, v8
	v_add_u32_e32 v2, 64, v2
	v_add_u32_e32 v8, 16, v8
	v_mov_b32_e32 v33, 0x3c00
	s_waitcnt lgkmcnt(0)
	v_perm_b32 v32, v37, v36, v57
	v_cndmask_b32_e32 v33, 0, v33, vcc
	s_nop 0
	v_cndmask_b32_e32 v32, 0, v32, vcc
	s_nop 1
	v_mfma_f32_32x32x16_f16 v[96:111], v[32:35], v[64:67], 0
	v_mfma_f32_32x32x16_f16 v[112:127], v[32:35], v[68:71], 0
	s_nop 10
	s_sub_u32 s45, s43, s44
	s_min_u32 s46, s45, 16
	s_add_i32 s46, s46, 3
	s_lshr_b32 s46, s46, 2
	s_cmp_eq_u32 s46, 4
	s_cbranch_scc1 .Ln4
	s_cmp_eq_u32 s46, 3
	s_cbranch_scc1 .Ln3
	s_cmp_eq_u32 s46, 2
	s_cbranch_scc1 .Ln2
.Ln1:
	v_add_f32_e64 v38, |v96|, |v97|
	v_add_f32_e64 v39, |v98|, |v99|
	v_add_f32_e32 v38, v38, v39
	v_add_f32_e32 v24, v24, v38
	s_nop 7
	v_mfma_f32_32x32x16_f16 v[96:111], v[32:35], v[72:75], 0
	v_add_f32_e64 v38, |v112|, |v113|
	v_add_f32_e64 v39, |v114|, |v115|
	v_add_f32_e32 v38, v38, v39
	v_add_f32_e32 v25, v25, v38
	s_nop 7
	v_mfma_f32_32x32x16_f16 v[112:127], v[32:35], v[76:79], 0
	v_add_f32_e64 v38, |v96|, |v97|
	v_add_f32_e64 v39, |v98|, |v99|
	v_add_f32_e32 v38, v38, v39
	v_add_f32_e32 v26, v26, v38
	s_nop 7
	v_mfma_f32_32x32x16_f16 v[96:111], v[32:35], v[80:83], 0
	v_add_f32_e64 v38, |v112|, |v113|
	v_add_f32_e64 v39, |v114|, |v115|
	v_add_f32_e32 v38, v38, v39
	v_add_f32_e32 v27, v27, v38
	s_nop 7
	v_mfma_f32_32x32x16_f16 v[112:127], v[32:35], v[84:87], 0
	v_add_f32_e64 v38, |v96|, |v97|
	v_add_f32_e64 v39, |v98|, |v99|
	v_add_f32_e32 v38, v38, v39
	v_add_f32_e32 v28, v28, v38
	s_nop 7
	v_mfma_f32_32x32x16_f16 v[96:111], v[32:35], v[88:91], 0
	v_add_f32_e64 v38, |v112|, |v113|
	v_add_f32_e64 v39, |v114|, |v115|
	v_add_f32_e32 v38, v38, v39
	v_add_f32_e32 v29, v29, v38
	s_nop 7
	v_mfma_f32_32x32x16_f16 v[112:127], v[32:35], v[92:95], 0
	v_add_f32_e64 v38, |v96|, |v97|
	v_add_f32_e64 v39, |v98|, |v99|
	v_add_f32_e32 v38, v38, v39
	v_add_f32_e32 v30, v30, v38
	s_nop 7
	v_add_f32_e64 v38, |v112|, |v113|
	v_add_f32_e64 v39, |v114|, |v115|
	v_add_f32_e32 v38, v38, v39
	v_add_f32_e32 v31, v31, v38
	s_nop 7
	s_branch .Lsub_next
.Ln2:
	v_add_f32_e64 v38, |v96|, |v97|
	v_add_f32_e64 v39, |v98|, |v99|
	v_add_f32_e64 v38, v38, |v100|
	v_add_f32_e64 v39, v39, |v101|
	v_add_f32_e64 v38, v38, |v102|
	v_add_f32_e64 v39, v39, |v103|
	v_add_f32_e32 v38, v38, v39
	v_add_f32_e32 v24, v24, v38
	s_nop 3
	v_mfma_f32_32x32x16_f16 v[96:111], v[32:35], v[72:75], 0
	v_add_f32_e64 v38, |v112|, |v113|
	v_add_f32_e64 v39, |v114|, |v115|
	v_add_f32_e64 v38, v38, |v116|
	v_add_f32_e64 v39, v39, |v117|
	v_add_f32_e64 v38, v38, |v118|
	v_add_f32_e64 v39, v39, |v119|
	v_add_f32_e32 v38, v38, v39
	v_add_f32_e32 v25, v25, v38
	s_nop 3
	v_mfma_f32_32x32x16_f16 v[112:127], v[32:35], v[76:79], 0
	v_add_f32_e64 v38, |v96|, |v97|
	v_add_f32_e64 v39, |v98|, |v99|
	v_add_f32_e64 v38, v38, |v100|
	v_add_f32_e64 v39, v39, |v101|
	v_add_f32_e64 v38, v38, |v102|
	v_add_f32_e64 v39, v39, |v103|
	v_add_f32_e32 v38, v38, v39
	v_add_f32_e32 v26, v26, v38
	s_nop 3
	v_mfma_f32_32x32x16_f16 v[96:111], v[32:35], v[80:83], 0
	v_add_f32_e64 v38, |v112|, |v113|
	v_add_f32_e64 v39, |v114|, |v115|
	v_add_f32_e64 v38, v38, |v116|
	v_add_f32_e64 v39, v39, |v117|
	v_add_f32_e64 v38, v38, |v118|
	v_add_f32_e64 v39, v39, |v119|
	v_add_f32_e32 v38, v38, v39
	v_add_f32_e32 v27, v27, v38
	s_nop 3
	v_mfma_f32_32x32x16_f16 v[112:127], v[32:35], v[84:87], 0
	v_add_f32_e64 v38, |v96|, |v97|
	v_add_f32_e64 v39, |v98|, |v99|
	v_add_f32_e64 v38, v38, |v100|
	v_add_f32_e64 v39, v39, |v101|
	v_add_f32_e64 v38, v38, |v102|
	v_add_f32_e64 v39, v39, |v103|
	v_add_f32_e32 v38, v38, v39
	v_add_f32_e32 v28, v28, v38
	s_nop 3
	v_mfma_f32_32x32x16_f16 v[96:111], v[32:35], v[88:91], 0
	v_add_f32_e64 v38, |v112|, |v113|
	v_add_f32_e64 v39, |v114|, |v115|
	v_add_f32_e64 v38, v38, |v116|
	v_add_f32_e64 v39, v39, |v117|
	v_add_f32_e64 v38, v38, |v118|
	v_add_f32_e64 v39, v39, |v119|
	v_add_f32_e32 v38, v38, v39
	v_add_f32_e32 v29, v29, v38
	s_nop 3
	v_mfma_f32_32x32x16_f16 v[112:127], v[32:35], v[92:95], 0
	v_add_f32_e64 v38, |v96|, |v97|
	v_add_f32_e64 v39, |v98|, |v99|
	v_add_f32_e64 v38, v38, |v100|
	v_add_f32_e64 v39, v39, |v101|
	v_add_f32_e64 v38, v38, |v102|
	v_add_f32_e64 v39, v39, |v103|
	v_add_f32_e32 v38, v38, v39
	v_add_f32_e32 v30, v30, v38
	s_nop 3
	v_add_f32_e64 v38, |v112|, |v113|
	v_add_f32_e64 v39, |v114|, |v115|
	v_add_f32_e64 v38, v38, |v116|
	v_add_f32_e64 v39, v39, |v117|
	v_add_f32_e64 v38, v38, |v118|
	v_add_f32_e64 v39, v39, |v119|
	v_add_f32_e32 v38, v38, v39
	v_add_f32_e32 v31, v31, v38
	s_nop 3
	s_branch .Lsub_next
.Ln3:
	v_add_f32_e64 v38, |v96|, |v97|
	v_add_f32_e64 v39, |v98|, |v99|
	v_add_f32_e64 v38, v38, |v100|
	v_add_f32_e64 v39, v39, |v101|
	v_add_f32_e64 v38, v38, |v102|
	v_add_f32_e64 v39, v39, |v103|
	v_add_f32_e64 v38, v38, |v104|
	v_add_f32_e64 v39, v39, |v105|
	v_add_f32_e64 v38, v38, |v106|
	v_add_f32_e64 v39, v39, |v107|
	v_add_f32_e32 v38, v38, v39
	v_add_f32_e32 v24, v24, v38
	v_mfma_f32_32x32x16_f16 v[96:111], v[32:35], v[72:75], 0
	v_add_f32_e64 v38, |v112|, |v113|
	v_add_f32_e64 v39, |v114|, |v115|
	v_add_f32_e64 v38, v38, |v116|
	v_add_f32_e64 v39, v39, |v117|
	v_add_f32_e64 v38, v38, |v118|
	v_add_f32_e64 v39, v39, |v119|
	v_add_f32_e64 v38, v38, |v120|
	v_add_f32_e64 v39, v39, |v121|
	v_add_f32_e64 v38, v38, |v122|
	v_add_f32_e64 v39, v39, |v123|
	v_add_f32_e32 v38, v38, v39
	v_add_f32_e32 v25, v25, v38
	v_mfma_f32_32x32x16_f16 v[112:127], v[32:35], v[76:79], 0
	v_add_f32_e64 v38, |v96|, |v97|
	v_add_f32_e64 v39, |v98|, |v99|
	v_add_f32_e64 v38, v38, |v100|
	v_add_f32_e64 v39, v39, |v101|
	v_add_f32_e64 v38, v38, |v102|
	v_add_f32_e64 v39, v39, |v103|
	v_add_f32_e64 v38, v38, |v104|
	v_add_f32_e64 v39, v39, |v105|
	v_add_f32_e64 v38, v38, |v106|
	v_add_f32_e64 v39, v39, |v107|
	v_add_f32_e32 v38, v38, v39
	v_add_f32_e32 v26, v26, v38
	v_mfma_f32_32x32x16_f16 v[96:111], v[32:35], v[80:83], 0
	v_add_f32_e64 v38, |v112|, |v113|
	v_add_f32_e64 v39, |v114|, |v115|
	v_add_f32_e64 v38, v38, |v116|
	v_add_f32_e64 v39, v39, |v117|
	v_add_f32_e64 v38, v38, |v118|
	v_add_f32_e64 v39, v39, |v119|
	v_add_f32_e64 v38, v38, |v120|
	v_add_f32_e64 v39, v39, |v121|
	v_add_f32_e64 v38, v38, |v122|
	v_add_f32_e64 v39, v39, |v123|
	v_add_f32_e32 v38, v38, v39
	v_add_f32_e32 v27, v27, v38
	v_mfma_f32_32x32x16_f16 v[112:127], v[32:35], v[84:87], 0
	v_add_f32_e64 v38, |v96|, |v97|
	v_add_f32_e64 v39, |v98|, |v99|
	v_add_f32_e64 v38, v38, |v100|
	v_add_f32_e64 v39, v39, |v101|
	v_add_f32_e64 v38, v38, |v102|
	v_add_f32_e64 v39, v39, |v103|
	v_add_f32_e64 v38, v38, |v104|
	v_add_f32_e64 v39, v39, |v105|
	v_add_f32_e64 v38, v38, |v106|
	v_add_f32_e64 v39, v39, |v107|
	v_add_f32_e32 v38, v38, v39
	v_add_f32_e32 v28, v28, v38
	v_mfma_f32_32x32x16_f16 v[96:111], v[32:35], v[88:91], 0
	v_add_f32_e64 v38, |v112|, |v113|
	v_add_f32_e64 v39, |v114|, |v115|
	v_add_f32_e64 v38, v38, |v116|
	v_add_f32_e64 v39, v39, |v117|
	v_add_f32_e64 v38, v38, |v118|
	v_add_f32_e64 v39, v39, |v119|
	v_add_f32_e64 v38, v38, |v120|
	v_add_f32_e64 v39, v39, |v121|
	v_add_f32_e64 v38, v38, |v122|
	v_add_f32_e64 v39, v39, |v123|
	v_add_f32_e32 v38, v38, v39
	v_add_f32_e32 v29, v29, v38
	v_mfma_f32_32x32x16_f16 v[112:127], v[32:35], v[92:95], 0
	v_add_f32_e64 v38, |v96|, |v97|
	v_add_f32_e64 v39, |v98|, |v99|
	v_add_f32_e64 v38, v38, |v100|
	v_add_f32_e64 v39, v39, |v101|
	v_add_f32_e64 v38, v38, |v102|
	v_add_f32_e64 v39, v39, |v103|
	v_add_f32_e64 v38, v38, |v104|
	v_add_f32_e64 v39, v39, |v105|
	v_add_f32_e64 v38, v38, |v106|
	v_add_f32_e64 v39, v39, |v107|
	v_add_f32_e32 v38, v38, v39
	v_add_f32_e32 v30, v30, v38
	v_add_f32_e64 v38, |v112|, |v113|
	v_add_f32_e64 v39, |v114|, |v115|
	v_add_f32_e64 v38, v38, |v116|
	v_add_f32_e64 v39, v39, |v117|
	v_add_f32_e64 v38, v38, |v118|
	v_add_f32_e64 v39, v39, |v119|
	v_add_f32_e64 v38, v38, |v120|
	v_add_f32_e64 v39, v39, |v121|
	v_add_f32_e64 v38, v38, |v122|
	v_add_f32_e64 v39, v39, |v123|
	v_add_f32_e32 v38, v38, v39
	v_add_f32_e32 v31, v31, v38
	s_branch .Lsub_next
.Ln4:
	v_add_f32_e64 v38, |v96|, |v97|
	v_add_f32_e64 v39, |v98|, |v99|
	v_add_f32_e64 v38, v38, |v100|
	v_add_f32_e64 v39, v39, |v101|
	v_add_f32_e64 v38, v38, |v102|
	v_add_f32_e64 v39, v39, |v103|
	v_add_f32_e64 v38, v38, |v104|
	v_add_f32_e64 v39, v39, |v105|
	v_add_f32_e64 v38, v38, |v106|
	v_add_f32_e64 v39, v39, |v107|
	v_add_f32_e64 v38, v38, |v108|
	v_add_f32_e64 v39, v39, |v109|
	v_add_f32_e64 v38, v38, |v110|
	v_add_f32_e64 v39, v39, |v111|
	v_add_f32_e32 v38, v38, v39
	v_add_f32_e32 v24, v24, v38
	v_mfma_f32_32x32x16_f16 v[96:111], v[32:35], v[72:75], 0
	v_add_f32_e64 v38, |v112|, |v113|
	v_add_f32_e64 v39, |v114|, |v115|
	v_add_f32_e64 v38, v38, |v116|
	v_add_f32_e64 v39, v39, |v117|
	v_add_f32_e64 v38, v38, |v118|
	v_add_f32_e64 v39, v39, |v119|
	v_add_f32_e64 v38, v38, |v120|
	v_add_f32_e64 v39, v39, |v121|
	v_add_f32_e64 v38, v38, |v122|
	v_add_f32_e64 v39, v39, |v123|
	v_add_f32_e64 v38, v38, |v124|
	v_add_f32_e64 v39, v39, |v125|
	v_add_f32_e64 v38, v38, |v126|
	v_add_f32_e64 v39, v39, |v127|
	v_add_f32_e32 v38, v38, v39
	v_add_f32_e32 v25, v25, v38
	v_mfma_f32_32x32x16_f16 v[112:127], v[32:35], v[76:79], 0
	v_add_f32_e64 v38, |v96|, |v97|
	v_add_f32_e64 v39, |v98|, |v99|
	v_add_f32_e64 v38, v38, |v100|
	v_add_f32_e64 v39, v39, |v101|
	v_add_f32_e64 v38, v38, |v102|
	v_add_f32_e64 v39, v39, |v103|
	v_add_f32_e64 v38, v38, |v104|
	v_add_f32_e64 v39, v39, |v105|
	v_add_f32_e64 v38, v38, |v106|
	v_add_f32_e64 v39, v39, |v107|
	v_add_f32_e64 v38, v38, |v108|
	v_add_f32_e64 v39, v39, |v109|
	v_add_f32_e64 v38, v38, |v110|
	v_add_f32_e64 v39, v39, |v111|
	v_add_f32_e32 v38, v38, v39
	v_add_f32_e32 v26, v26, v38
	v_mfma_f32_32x32x16_f16 v[96:111], v[32:35], v[80:83], 0
	v_add_f32_e64 v38, |v112|, |v113|
	v_add_f32_e64 v39, |v114|, |v115|
	v_add_f32_e64 v38, v38, |v116|
	v_add_f32_e64 v39, v39, |v117|
	v_add_f32_e64 v38, v38, |v118|
	v_add_f32_e64 v39, v39, |v119|
	v_add_f32_e64 v38, v38, |v120|
	v_add_f32_e64 v39, v39, |v121|
	v_add_f32_e64 v38, v38, |v122|
	v_add_f32_e64 v39, v39, |v123|
	v_add_f32_e64 v38, v38, |v124|
	v_add_f32_e64 v39, v39, |v125|
	v_add_f32_e64 v38, v38, |v126|
	v_add_f32_e64 v39, v39, |v127|
	v_add_f32_e32 v38, v38, v39
	v_add_f32_e32 v27, v27, v38
	v_mfma_f32_32x32x16_f16 v[112:127], v[32:35], v[84:87], 0
	v_add_f32_e64 v38, |v96|, |v97|
	v_add_f32_e64 v39, |v98|, |v99|
	v_add_f32_e64 v38, v38, |v100|
	v_add_f32_e64 v39, v39, |v101|
	v_add_f32_e64 v38, v38, |v102|
	v_add_f32_e64 v39, v39, |v103|
	v_add_f32_e64 v38, v38, |v104|
	v_add_f32_e64 v39, v39, |v105|
	v_add_f32_e64 v38, v38, |v106|
	v_add_f32_e64 v39, v39, |v107|
	v_add_f32_e64 v38, v38, |v108|
	v_add_f32_e64 v39, v39, |v109|
	v_add_f32_e64 v38, v38, |v110|
	v_add_f32_e64 v39, v39, |v111|
	v_add_f32_e32 v38, v38, v39
	v_add_f32_e32 v28, v28, v38
	v_mfma_f32_32x32x16_f16 v[96:111], v[32:35], v[88:91], 0
	v_add_f32_e64 v38, |v112|, |v113|
	v_add_f32_e64 v39, |v114|, |v115|
	v_add_f32_e64 v38, v38, |v116|
	v_add_f32_e64 v39, v39, |v117|
	v_add_f32_e64 v38, v38, |v118|
	v_add_f32_e64 v39, v39, |v119|
	v_add_f32_e64 v38, v38, |v120|
	v_add_f32_e64 v39, v39, |v121|
	v_add_f32_e64 v38, v38, |v122|
	v_add_f32_e64 v39, v39, |v123|
	v_add_f32_e64 v38, v38, |v124|
	v_add_f32_e64 v39, v39, |v125|
	v_add_f32_e64 v38, v38, |v126|
	v_add_f32_e64 v39, v39, |v127|
	v_add_f32_e32 v38, v38, v39
	v_add_f32_e32 v29, v29, v38
	v_mfma_f32_32x32x16_f16 v[112:127], v[32:35], v[92:95], 0
	v_add_f32_e64 v38, |v96|, |v97|
	v_add_f32_e64 v39, |v98|, |v99|
	v_add_f32_e64 v38, v38, |v100|
	v_add_f32_e64 v39, v39, |v101|
	v_add_f32_e64 v38, v38, |v102|
	v_add_f32_e64 v39, v39, |v103|
	v_add_f32_e64 v38, v38, |v104|
	v_add_f32_e64 v39, v39, |v105|
	v_add_f32_e64 v38, v38, |v106|
	v_add_f32_e64 v39, v39, |v107|
	v_add_f32_e64 v38, v38, |v108|
	v_add_f32_e64 v39, v39, |v109|
	v_add_f32_e64 v38, v38, |v110|
	v_add_f32_e64 v39, v39, |v111|
	v_add_f32_e32 v38, v38, v39
	v_add_f32_e32 v30, v30, v38
	v_add_f32_e64 v38, |v112|, |v113|
	v_add_f32_e64 v39, |v114|, |v115|
	v_add_f32_e64 v38, v38, |v116|
	v_add_f32_e64 v39, v39, |v117|
	v_add_f32_e64 v38, v38, |v118|
	v_add_f32_e64 v39, v39, |v119|
	v_add_f32_e64 v38, v38, |v120|
	v_add_f32_e64 v39, v39, |v121|
	v_add_f32_e64 v38, v38, |v122|
	v_add_f32_e64 v39, v39, |v123|
	v_add_f32_e64 v38, v38, |v124|
	v_add_f32_e64 v39, v39, |v125|
	v_add_f32_e64 v38, v38, |v126|
	v_add_f32_e64 v39, v39, |v127|
	v_add_f32_e32 v38, v38, v39
	v_add_f32_e32 v31, v31, v38
.Lsub_next:
	s_add_i32 s44, s44, 16
	s_cmp_lt_u32 s44, s43
	s_cbranch_scc1 .Lsub

.Lp_zero:
	v_mov_b32_e32 v24, 0
	v_mov_b32_e32 v25, 0
	v_mov_b32_e32 v26, 0
	v_mov_b32_e32 v27, 0
	v_mov_b32_e32 v28, 0
	v_mov_b32_e32 v29, 0
	v_mov_b32_e32 v30, 0
	v_mov_b32_e32 v31, 0
	s_branch .Lp_fin
